# deferred weight-conversion split 3400 + 1700, idle-slot quotas 6/10/8/10
# speedup vs baseline: 1.0021x; 1.0021x over previous
; #define SEAM(k) do { if (IN(k) && IN((k) + 1)) xcd_barrier(bar); \
;         if (PROBE_MASK) { const unsigned long long t_ = __builtin_amdgcn_s_memrealtime(); if ((PROBE_MASK >> (k)) & 1u) pr_acc += t_ - pr_t0; pr_t0 = t_; } } while (0)
; __device__ __forceinline__ void convert_deferred(const Ptrs& P, unsigned char* lds, int quota) {
;     const int tid = threadIdx.x, wid = tid >> 6, lane = tid & 63;
;     float* tile = (float*)lds;
;     volatile __attribute__((address_space(3))) int* slot = (volatile __attribute__((address_space(3))) int*)((__attribute__((address_space(3))) unsigned char*)lds + 131072 + 320 + 11000);
;     unsigned* q = (unsigned*)(P.ws + WS_CTL) + CW_DEFQ;
;     for (int n = 0; n < quota; ++n) {
;         __syncthreads();
;         if (tid == 0) *slot = (int)atomicAdd(q, 1u);
;         __syncthreads();
;         const int t = *slot;
;         if (t >= DEF_GU + DEF_DN) break;
;         const bool gu = t < DEF_GU;
;         const float* src = gu ? P.in[34] : P.in[36]; bf16* dst = (bf16*)(P.ws + (gu ? WS_WGU : WS_WDN));
;         const int N = gu ? 2048 : 1024, ntn = N / 256, it = gu ? 2 * NE * 16 * 8 - DEF_GU + t : 2 * NE * 16 * 4 - DEF_DN + (t - DEF_GU);
; __global__ void __launch_bounds__(NT, 2) mega(Args args) {
;     ...
;         if (IDLE_LAST(68 * 4)) convert_deferred(P, lds, 4); } SEAM(6);
.LBB0_1286:
	s_abs_i32 s3, s62
	v_cvt_f32_u32_e32 v2, s3
	s_sub_i32 s4, 0, s3
	s_mov_b32 s5, 0
	v_rcp_iflag_f32_e32 v2, v2
	s_nop 0
	v_mul_f32_e32 v2, 0x4f7ffffe, v2
	v_cvt_u32_f32_e32 v2, v2
	s_nop 0
	v_readfirstlane_b32 s6, v2
	s_mul_i32 s4, s4, s6
	s_mul_hi_u32 s4, s6, s4
	s_add_i32 s6, s6, s4
	s_mul_hi_u32 s4, s6, 0x110
	s_mul_i32 s4, s4, s3
	s_sub_i32 s4, 0x110, s4
	s_sub_i32 s6, s4, s3
	s_cmp_ge_u32 s4, s3
	s_cselect_b32 s4, s6, s4
	s_sub_i32 s6, s4, s3
	s_cmp_ge_u32 s4, s3
	s_cselect_b32 s3, s6, s4
	s_cmp_eq_u32 s3, 0
	s_cselect_b64 s[6:7], -1, 0
	s_cmp_lt_i32 s2, s3
	s_cselect_b64 s[8:9], -1, 0
	s_or_b64 s[6:7], s[6:7], s[8:9]
	s_and_b64 vcc, exec, s[6:7]
	s_cbranch_vccnz .LBB0_1296
	v_and_b32_e32 v2, 0x7c, v188
	v_lshlrev_b32_e32 v3, 5, v0
	s_movk_i32 s3, 0x400
	v_and_or_b32 v12, v3, s3, v2
	v_bfe_u32 v2, v0, 3, 3
	v_lshl_or_b32 v4, v1, 5, v2
	v_lshlrev_b32_e32 v2, 3, v0
	v_lshl_add_u32 v11, v182, 4, 0
	v_and_b32_e32 v2, 56, v2
	v_mul_u32_u24_e32 v16, 0x2020, v1
	v_mov_b32_e32 v3, 0
	v_lshl_add_u32 v27, v4, 2, 0
	v_mul_u32_u24_e32 v28, 0x404, v2
	v_lshlrev_b32_e32 v10, 6, v4
	s_add_i32 s12, 0, 0x22c38
	v_add_u32_e32 v16, v11, v16
	v_and_b32_e32 v13, 0xfc, v188
	v_and_b32_e32 v14, 56, v185
	s_mov_b32 s3, 10
	v_or_b32_e32 v4, 0x200, v10
	v_mov_b32_e32 v5, v3
	v_or_b32_e32 v6, 0x400, v10
	v_mov_b32_e32 v7, v3
	v_or_b32_e32 v8, 0x600, v10
	v_mov_b32_e32 v9, v3
	v_mov_b32_e32 v15, s12
	s_movk_i32 s13, 0x13eb
	s_movk_i32 s14, 0x800
	s_mov_b32 s15, 0x1104e000
	s_movk_i32 s16, -1004
	v_add_u32_e32 v17, 0x404, v16
	v_add_u32_e32 v18, 0x40c, v16
	v_add_u32_e32 v19, 0x808, v16
	v_add_u32_e32 v20, 0xc0c, v16
	v_add_u32_e32 v21, 0xc14, v16
	v_add_u32_e32 v22, 0x1414, v16
	v_add_u32_e32 v23, 0x141c, v16
	v_add_u32_e32 v24, 0x1818, v16
	v_add_u32_e32 v25, 0x1c1c, v16
	v_add_u32_e32 v26, 0x1c24, v16
	v_lshlrev_b32_e32 v2, 1, v2
	v_add_u32_e32 v27, v27, v28
	v_lshlrev_b32_e32 v10, 1, v10
	s_branch .LBB0_1289
